# baseline (speedup 1.0000x reference)
_Z13select_kernelPK15HIP_vector_typeIjLj2EEPKfPf:
	s_lshr_b32 s3, s2, 3
	s_lshl_b32 s4, s2, 2
	s_mul_hi_u32 s2, s2, 0xaaaaaaab
	s_load_dwordx2 s[38:39], s[0:1], 0x0
	s_load_dwordx2 s[36:37], s[0:1], 0x10
	s_and_b32 s33, s4, 28
	s_lshr_b32 s2, s2, 5
	s_add_i32 s33, s33, s2
	s_mul_hi_u32 s2, s3, 0x2aaaaaab
	s_mul_i32 s2, s2, 6
	s_sub_i32 s46, s3, s2
	s_cmp_lg_u32 s46, 0
	s_cbranch_scc0 .LBB1_47
	s_load_dwordx2 s[40:41], s[0:1], 0x8
	s_movk_i32 s0, 0x140
	v_cmp_gt_u32_e64 s[2:3], s0, v0
	s_mov_b64 s[0:1], 0
	s_and_saveexec_b64 s[4:5], s[2:3]
	s_cbranch_execz .LBB1_3
	s_mul_i32 s0, s33, 0x1388
	v_add_u32_e32 v2, s0, v0
	v_mov_b32_e32 v3, 0
	s_waitcnt lgkmcnt(0)
	v_lshl_add_u64 v[2:3], v[2:3], 3, s[38:39]
	global_load_dword v57, v[2:3], off offset:4
.LBB1_3:
	s_or_b64 exec, exec, s[4:5]
	s_add_i32 s47, s46, -1
	v_lshrrev_b32_e32 v30, 4, v0
	v_lshl_or_b32 v1, s47, 6, v30
	v_lshrrev_b16_e32 v2, 2, v1
	v_mul_u32_u24_e32 v2, 0x147b, v2
	v_lshrrev_b32_e32 v2, 17, v2
	s_movk_i32 s4, 0xff9c
	v_bfe_u32 v36, v0, 1, 3
	v_mad_i32_i24 v1, v2, s4, v1
	v_lshl_or_b32 v14, v2, 3, v36
	v_lshlrev_b32_e32 v2, 2, v0
	v_and_b32_e32 v37, 4, v2
	v_lshl_or_b32 v2, v1, 3, v37
	s_mul_i32 s43, s33, 3
	v_mov_b32_e32 v15, 0
	v_mov_b32_e32 v1, 0x190
	v_mad_u64_u32 v[4:5], s[4:5], s43, v1, v[14:15]
	s_movk_i32 s6, 0xc80
	s_waitcnt lgkmcnt(0)
	v_mov_b64_e32 v[6:7], s[40:41]
	v_mad_u64_u32 v[6:7], s[4:5], v4, s6, v[6:7]
	v_mad_u32_u24 v7, v5, s6, v7
	v_ashrrev_i32_e32 v3, 31, v2
	v_lshl_add_u64 v[10:11], v[2:3], 2, v[6:7]
	s_mov_b32 s4, 0x138000
	v_add_co_u32_e32 v12, vcc, s4, v10
	v_and_b32_e32 v1, 63, v0
	s_nop 0
	v_addc_co_u32_e32 v13, vcc, 0, v11, vcc
	global_load_dwordx4 v[2:5], v[10:11], off nt
	global_load_dwordx4 v[6:9], v[12:13], off offset:2048 nt
	v_add_co_u32_e32 v10, vcc, 0x271000, v10
	s_nop 1
	v_addc_co_u32_e32 v11, vcc, 0, v11, vcc
	global_load_dwordx4 v[10:13], v[10:11], off nt
	v_cmp_eq_u32_e64 s[0:1], 0, v1
	v_lshrrev_b32_e32 v39, 6, v0
	s_waitcnt vmcnt(3)
	v_cmp_gt_u32_e64 s[4:5], 64, v57
	s_and_b64 s[4:5], s[4:5], s[2:3]
	s_and_b64 s[6:7], s[2:3], s[0:1]
	s_and_saveexec_b64 s[2:3], s[6:7]
	v_lshlrev_b32_e32 v14, 3, v39
	v_mov_b64_e32 v[16:17], s[4:5]
	ds_write_b64 v14, v[16:17] offset:48368
	s_or_b64 exec, exec, s[2:3]
	s_waitcnt lgkmcnt(0)
	s_barrier
	ds_read_b128 v[16:19], v15 offset:48368
	ds_read_b128 v[20:23], v15 offset:48384
	ds_read_b64 v[14:15], v15 offset:48400
	s_movk_i32 s2, 0x12c
	s_waitcnt lgkmcnt(2)
	v_bcnt_u32_b32 v16, v16, 0
	v_bcnt_u32_b32 v31, v17, v16
	v_bcnt_u32_b32 v16, v18, 0
	v_bcnt_u32_b32 v33, v19, v16
	s_waitcnt lgkmcnt(1)
	v_bcnt_u32_b32 v17, v20, 0
	v_add_u32_e32 v16, v33, v31
	v_bcnt_u32_b32 v34, v21, v17
	v_bcnt_u32_b32 v17, v22, 0
	v_add_u32_e32 v16, v16, v34
	v_bcnt_u32_b32 v35, v23, v17
	s_waitcnt lgkmcnt(0)
	v_bcnt_u32_b32 v14, v14, 0
	v_add_u32_e32 v16, v16, v35
	v_bcnt_u32_b32 v14, v15, v14
	v_add_u32_e32 v14, v16, v14
	v_cmp_gt_u32_e32 vcc, s2, v14
	s_cbranch_vccnz .Lk2_generic

.LBB1_46:
	s_or_b64 exec, exec, s[0:1]
	s_endpgm
.Lk2_generic:
	s_mul_i32 s48, s33, 0x1388
	v_add_u32_e32 v14, s48, v0
	v_mov_b32_e32 v15, 0
	v_lshl_add_u64 v[16:17], v[14:15], 3, s[38:39]
	s_barrier
	global_load_dword v14, v[16:17], off offset:4
	v_lshlrev_b32_e32 v38, 2, v39
	s_waitcnt vmcnt(0)
	v_cmp_gt_u32_e32 vcc, 64, v14
	s_and_saveexec_b64 s[2:3], s[0:1]
	s_bcnt1_i32_b64 s4, vcc
	v_mov_b32_e32 v14, s4
	ds_write_b32 v38, v14 offset:48224
	s_or_b64 exec, exec, s[2:3]
	v_lshlrev_b64 v[16:17], v1, -1
	v_not_b32_e32 v32, v16
	v_not_b32_e32 v1, v17
	v_and_b32_e32 v16, vcc_lo, v32
	v_and_b32_e32 v14, vcc_hi, v1
	v_bcnt_u32_b32 v16, v16, 0
	v_bcnt_u32_b32 v40, v14, v16
	s_waitcnt lgkmcnt(0)
	s_barrier
	ds_read_b128 v[26:29], v15 offset:48224
	ds_read_b128 v[22:25], v15 offset:48240
	ds_read_b128 v[18:21], v15 offset:48256
	ds_read_b128 v[14:17], v15 offset:48272
	s_movk_i32 s4, 0x7f
	s_movk_i32 s6, 0xbf
	v_cmp_gt_u32_e64 s[2:3], 64, v0
	s_movk_i32 s8, 0xff
	s_movk_i32 s10, 0x13f
	s_waitcnt lgkmcnt(3)
	v_cndmask_b32_e64 v41, v26, 0, s[2:3]
	v_cmp_lt_u32_e64 s[4:5], s4, v0
	v_cmp_lt_u32_e64 s[6:7], s6, v0
	s_movk_i32 s12, 0x17f
	s_movk_i32 s14, 0x1bf
	v_cndmask_b32_e64 v42, 0, v27, s[4:5]
	v_cndmask_b32_e64 v43, 0, v28, s[6:7]
	v_cmp_lt_u32_e64 s[8:9], s8, v0
	v_cmp_lt_u32_e64 s[10:11], s10, v0
	v_add_u32_e32 v40, v41, v40
	s_movk_i32 s16, 0x1ff
	s_movk_i32 s18, 0x23f
	v_cndmask_b32_e64 v44, 0, v29, s[8:9]
	s_waitcnt lgkmcnt(2)
	v_cndmask_b32_e64 v45, 0, v22, s[10:11]
	v_cmp_lt_u32_e64 s[12:13], s12, v0
	v_cmp_lt_u32_e64 s[14:15], s14, v0
	v_add3_u32 v40, v40, v42, v43
	s_movk_i32 s20, 0x27f
	s_movk_i32 s22, 0x2bf
	v_cndmask_b32_e64 v46, 0, v23, s[12:13]
	v_cndmask_b32_e64 v47, 0, v24, s[14:15]
	v_cmp_lt_u32_e64 s[16:17], s16, v0
	v_cmp_lt_u32_e64 s[18:19], s18, v0
	v_add3_u32 v40, v40, v44, v45
	s_movk_i32 s24, 0x2ff
	s_movk_i32 s26, 0x33f
	v_cndmask_b32_e64 v48, 0, v25, s[16:17]
	s_waitcnt lgkmcnt(1)
	v_cndmask_b32_e64 v49, 0, v18, s[18:19]
	v_cmp_lt_u32_e64 s[20:21], s20, v0
	v_cmp_lt_u32_e64 s[22:23], s22, v0
	v_add3_u32 v40, v40, v46, v47
	s_movk_i32 s28, 0x37f
	v_cndmask_b32_e64 v50, 0, v19, s[20:21]
	v_cndmask_b32_e64 v51, 0, v20, s[22:23]
	v_cmp_lt_u32_e64 s[24:25], s24, v0
	v_cmp_lt_u32_e64 s[26:27], s26, v0
	v_add3_u32 v40, v40, v48, v49
	v_cndmask_b32_e64 v52, 0, v21, s[24:25]
	s_waitcnt lgkmcnt(0)
	v_cndmask_b32_e64 v53, 0, v14, s[26:27]
	v_cmp_lt_u32_e64 s[28:29], s28, v0
	v_cmp_eq_u32_e64 s[30:31], 15, v39
	v_add3_u32 v40, v40, v50, v51
	v_cndmask_b32_e64 v54, 0, v15, s[28:29]
	v_cndmask_b32_e64 v39, 0, v16, s[30:31]
	v_add3_u32 v40, v40, v52, v53
	v_add3_u32 v39, v40, v54, v39
	s_movk_i32 s44, 0x12c
	v_cmp_gt_i32_e64 s[34:35], s44, v39
	s_and_b64 s[50:51], vcc, s[34:35]
	s_and_saveexec_b64 s[34:35], s[50:51]
	v_lshlrev_b32_e32 v39, 2, v39
	ds_write_b32 v39, v0 offset:48464
	s_or_b64 exec, exec, s[34:35]
	v_add_u32_e32 v26, v27, v26
	v_add_u32_e32 v26, v26, v28
	v_add_u32_e32 v26, v26, v29
	v_add_u32_e32 v22, v26, v22
	v_add_u32_e32 v22, v22, v23
	v_add_u32_e32 v22, v22, v24
	v_add_u32_e32 v22, v22, v25
	v_add_u32_e32 v18, v22, v18
	v_add_u32_e32 v18, v18, v19
	v_add_u32_e32 v18, v18, v20
	v_add_u32_e32 v18, v18, v21
	v_add_u32_e32 v14, v18, v14
	v_add_u32_e32 v14, v14, v15
	v_add_u32_e32 v14, v14, v16
	v_add_u32_e32 v39, v14, v17
	v_cmp_gt_i32_e32 vcc, s44, v39
	s_mul_i32 s42, s33, 0x4b0
	s_mul_hi_u32 s43, s43, 0x190
	s_waitcnt lgkmcnt(0)
	s_barrier
	s_cbranch_vccz .LBB1_33
	v_or_b32_e32 v40, 0x400, v0
	v_add_u32_e32 v14, s48, v40
	v_mov_b32_e32 v15, 0
	v_lshl_add_u64 v[16:17], v[14:15], 3, s[38:39]
	global_load_dword v14, v[16:17], off offset:4
	s_waitcnt vmcnt(0)
	v_cmp_gt_u32_e32 vcc, 64, v14
	s_and_saveexec_b64 s[34:35], s[0:1]
	s_bcnt1_i32_b64 s44, vcc
	v_mov_b32_e32 v14, s44
	ds_write_b32 v38, v14 offset:48224
	s_or_b64 exec, exec, s[34:35]
	s_waitcnt lgkmcnt(0)
	s_barrier
	ds_read_b128 v[26:29], v15 offset:48224
	v_and_b32_e32 v16, vcc_lo, v32
	v_and_b32_e32 v14, vcc_hi, v1
	v_bcnt_u32_b32 v16, v16, 0
	v_bcnt_u32_b32 v41, v14, v16
	ds_read_b128 v[22:25], v15 offset:48240
	ds_read_b128 v[18:21], v15 offset:48256
	ds_read_b128 v[14:17], v15 offset:48272
	s_waitcnt lgkmcnt(3)
	v_cndmask_b32_e64 v42, v26, 0, s[2:3]
	v_cndmask_b32_e64 v43, 0, v27, s[4:5]
	v_cndmask_b32_e64 v44, 0, v28, s[6:7]
	v_add3_u32 v41, v39, v41, v42
	v_cndmask_b32_e64 v45, 0, v29, s[8:9]
	s_waitcnt lgkmcnt(2)
	v_cndmask_b32_e64 v46, 0, v22, s[10:11]
	v_add3_u32 v41, v41, v43, v44
	v_cndmask_b32_e64 v47, 0, v23, s[12:13]
	v_cndmask_b32_e64 v48, 0, v24, s[14:15]
	v_add3_u32 v41, v41, v45, v46
	v_cndmask_b32_e64 v49, 0, v25, s[16:17]
	s_waitcnt lgkmcnt(1)
	v_cndmask_b32_e64 v50, 0, v18, s[18:19]
	v_add3_u32 v41, v41, v47, v48
	v_cndmask_b32_e64 v51, 0, v19, s[20:21]
	v_cndmask_b32_e64 v52, 0, v20, s[22:23]
	v_add3_u32 v41, v41, v49, v50
	v_cndmask_b32_e64 v53, 0, v21, s[24:25]
	s_waitcnt lgkmcnt(0)
	v_cndmask_b32_e64 v54, 0, v14, s[26:27]
	v_add3_u32 v41, v41, v51, v52
	v_cndmask_b32_e64 v55, 0, v15, s[28:29]
	v_cndmask_b32_e64 v56, 0, v16, s[30:31]
	v_add3_u32 v41, v41, v53, v54
	v_add3_u32 v41, v41, v55, v56
	s_movk_i32 s34, 0x12c
	v_cmp_gt_i32_e64 s[34:35], s34, v41
	s_and_b64 s[44:45], vcc, s[34:35]
	s_and_saveexec_b64 s[34:35], s[44:45]
	v_lshlrev_b32_e32 v41, 2, v41
	ds_write_b32 v41, v40 offset:48464
	s_or_b64 exec, exec, s[34:35]
	v_add_u32_e32 v26, v26, v39
	v_add_u32_e32 v26, v26, v27
	v_add_u32_e32 v26, v26, v28
	v_add_u32_e32 v26, v26, v29
	v_add_u32_e32 v22, v26, v22
	v_add_u32_e32 v22, v22, v23
	v_add_u32_e32 v22, v22, v24
	v_add_u32_e32 v22, v22, v25
	v_add_u32_e32 v18, v22, v18
	v_add_u32_e32 v18, v18, v19
	v_add_u32_e32 v18, v18, v20
	v_add_u32_e32 v18, v18, v21
	v_add_u32_e32 v14, v18, v14
	v_add_u32_e32 v14, v14, v15
	v_add_u32_e32 v14, v14, v16
	v_add_u32_e32 v39, v14, v17
	s_movk_i32 s34, 0x12b
	v_cmp_lt_i32_e32 vcc, s34, v39
	s_waitcnt lgkmcnt(0)
	s_barrier
	s_cbranch_vccnz .LBB1_33
	v_or_b32_e32 v40, 0x800, v0
	v_add_u32_e32 v14, s48, v40
	v_mov_b32_e32 v15, 0
	v_lshl_add_u64 v[16:17], v[14:15], 3, s[38:39]
	global_load_dword v14, v[16:17], off offset:4
	s_waitcnt vmcnt(0)
	v_cmp_gt_u32_e32 vcc, 64, v14
	s_and_saveexec_b64 s[34:35], s[0:1]
	s_bcnt1_i32_b64 s44, vcc
	v_mov_b32_e32 v14, s44
	ds_write_b32 v38, v14 offset:48224
	s_or_b64 exec, exec, s[34:35]
	s_waitcnt lgkmcnt(0)
	s_barrier
	ds_read_b128 v[26:29], v15 offset:48224
	v_and_b32_e32 v16, vcc_lo, v32
	v_and_b32_e32 v14, vcc_hi, v1
	v_bcnt_u32_b32 v16, v16, 0
	v_bcnt_u32_b32 v41, v14, v16
	ds_read_b128 v[22:25], v15 offset:48240
	ds_read_b128 v[18:21], v15 offset:48256
	ds_read_b128 v[14:17], v15 offset:48272
	s_waitcnt lgkmcnt(3)
	v_cndmask_b32_e64 v42, v26, 0, s[2:3]
	v_cndmask_b32_e64 v43, 0, v27, s[4:5]
	v_cndmask_b32_e64 v44, 0, v28, s[6:7]
	v_add3_u32 v41, v39, v41, v42
	v_cndmask_b32_e64 v45, 0, v29, s[8:9]
	s_waitcnt lgkmcnt(2)
	v_cndmask_b32_e64 v46, 0, v22, s[10:11]
	v_add3_u32 v41, v41, v43, v44
	v_cndmask_b32_e64 v47, 0, v23, s[12:13]
	v_cndmask_b32_e64 v48, 0, v24, s[14:15]
	v_add3_u32 v41, v41, v45, v46
	v_cndmask_b32_e64 v49, 0, v25, s[16:17]
	s_waitcnt lgkmcnt(1)
	v_cndmask_b32_e64 v50, 0, v18, s[18:19]
	v_add3_u32 v41, v41, v47, v48
	v_cndmask_b32_e64 v51, 0, v19, s[20:21]
	v_cndmask_b32_e64 v52, 0, v20, s[22:23]
	v_add3_u32 v41, v41, v49, v50
	v_cndmask_b32_e64 v53, 0, v21, s[24:25]
	s_waitcnt lgkmcnt(0)
	v_cndmask_b32_e64 v54, 0, v14, s[26:27]
	v_add3_u32 v41, v41, v51, v52
	v_cndmask_b32_e64 v55, 0, v15, s[28:29]
	v_cndmask_b32_e64 v56, 0, v16, s[30:31]
	v_add3_u32 v41, v41, v53, v54
	v_add3_u32 v41, v41, v55, v56
	s_movk_i32 s34, 0x12c
	v_cmp_gt_i32_e64 s[34:35], s34, v41
	s_and_b64 s[44:45], vcc, s[34:35]
	s_and_saveexec_b64 s[34:35], s[44:45]
	v_lshlrev_b32_e32 v41, 2, v41
	ds_write_b32 v41, v40 offset:48464
	s_or_b64 exec, exec, s[34:35]
	v_add_u32_e32 v26, v26, v39
	v_add_u32_e32 v26, v26, v27
	v_add_u32_e32 v26, v26, v28
	v_add_u32_e32 v26, v26, v29
	v_add_u32_e32 v22, v26, v22
	v_add_u32_e32 v22, v22, v23
	v_add_u32_e32 v22, v22, v24
	v_add_u32_e32 v22, v22, v25
	v_add_u32_e32 v18, v22, v18
	v_add_u32_e32 v18, v18, v19
	v_add_u32_e32 v18, v18, v20
	v_add_u32_e32 v18, v18, v21
	v_add_u32_e32 v14, v18, v14
	v_add_u32_e32 v14, v14, v15
	v_add_u32_e32 v14, v14, v16
	v_add_u32_e32 v39, v14, v17
	s_movk_i32 s34, 0x12b
	v_cmp_lt_i32_e32 vcc, s34, v39
	s_waitcnt lgkmcnt(0)
	s_barrier
	s_cbranch_vccnz .LBB1_33
	v_or_b32_e32 v40, 0xc00, v0
	v_add_u32_e32 v14, s48, v40
	v_mov_b32_e32 v15, 0
	v_lshl_add_u64 v[16:17], v[14:15], 3, s[38:39]
	global_load_dword v14, v[16:17], off offset:4
	s_waitcnt vmcnt(0)
	v_cmp_gt_u32_e32 vcc, 64, v14
	s_and_saveexec_b64 s[34:35], s[0:1]
	s_bcnt1_i32_b64 s44, vcc
	v_mov_b32_e32 v14, s44
	ds_write_b32 v38, v14 offset:48224
	s_or_b64 exec, exec, s[34:35]
	s_waitcnt lgkmcnt(0)
	s_barrier
	ds_read_b128 v[26:29], v15 offset:48224
	v_and_b32_e32 v16, vcc_lo, v32
	v_and_b32_e32 v14, vcc_hi, v1
	v_bcnt_u32_b32 v16, v16, 0
	v_bcnt_u32_b32 v41, v14, v16
	ds_read_b128 v[22:25], v15 offset:48240
	ds_read_b128 v[18:21], v15 offset:48256
	ds_read_b128 v[14:17], v15 offset:48272
	s_waitcnt lgkmcnt(3)
	v_cndmask_b32_e64 v42, v26, 0, s[2:3]
	v_cndmask_b32_e64 v43, 0, v27, s[4:5]
	v_cndmask_b32_e64 v44, 0, v28, s[6:7]
	v_add3_u32 v41, v39, v41, v42
	v_cndmask_b32_e64 v45, 0, v29, s[8:9]
	s_waitcnt lgkmcnt(2)
	v_cndmask_b32_e64 v46, 0, v22, s[10:11]
	v_add3_u32 v41, v41, v43, v44
	v_cndmask_b32_e64 v47, 0, v23, s[12:13]
	v_cndmask_b32_e64 v48, 0, v24, s[14:15]
	v_add3_u32 v41, v41, v45, v46
	v_cndmask_b32_e64 v49, 0, v25, s[16:17]
	s_waitcnt lgkmcnt(1)
	v_cndmask_b32_e64 v50, 0, v18, s[18:19]
	v_add3_u32 v41, v41, v47, v48
	v_cndmask_b32_e64 v51, 0, v19, s[20:21]
	v_cndmask_b32_e64 v52, 0, v20, s[22:23]
	v_add3_u32 v41, v41, v49, v50
	v_cndmask_b32_e64 v53, 0, v21, s[24:25]
	s_waitcnt lgkmcnt(0)
	v_cndmask_b32_e64 v54, 0, v14, s[26:27]
	v_add3_u32 v41, v41, v51, v52
	v_cndmask_b32_e64 v55, 0, v15, s[28:29]
	v_cndmask_b32_e64 v56, 0, v16, s[30:31]
	v_add3_u32 v41, v41, v53, v54
	v_add3_u32 v41, v41, v55, v56
	s_movk_i32 s34, 0x12c
	v_cmp_gt_i32_e64 s[34:35], s34, v41
	s_and_b64 s[44:45], vcc, s[34:35]
	s_and_saveexec_b64 s[34:35], s[44:45]
	v_lshlrev_b32_e32 v41, 2, v41
	ds_write_b32 v41, v40 offset:48464
	s_or_b64 exec, exec, s[34:35]
	v_add_u32_e32 v26, v26, v39
	v_add_u32_e32 v26, v26, v27
	v_add_u32_e32 v26, v26, v28
	v_add_u32_e32 v26, v26, v29
	v_add_u32_e32 v22, v26, v22
	v_add_u32_e32 v22, v22, v23
	v_add_u32_e32 v22, v22, v24
	v_add_u32_e32 v22, v22, v25
	v_add_u32_e32 v18, v22, v18
	v_add_u32_e32 v18, v18, v19
	v_add_u32_e32 v18, v18, v20
	v_add_u32_e32 v18, v18, v21
	v_add_u32_e32 v14, v18, v14
	v_add_u32_e32 v14, v14, v15
	v_add_u32_e32 v14, v14, v16
	v_add_u32_e32 v39, v14, v17
	s_movk_i32 s34, 0x12b
	v_cmp_lt_i32_e32 vcc, s34, v39
	s_waitcnt lgkmcnt(0)
	s_barrier
	s_cbranch_vccnz .LBB1_33
	v_or_b32_e32 v40, 0x1000, v0
	s_movk_i32 s34, 0x1388
	v_cmp_gt_u32_e32 vcc, s34, v40
	s_mov_b64 s[34:35], 0
	s_and_saveexec_b64 s[44:45], vcc
	s_cbranch_execz .LBB1_28
	v_add_u32_e32 v14, s48, v40
	v_mov_b32_e32 v15, 0
	v_lshl_add_u64 v[14:15], v[14:15], 3, s[38:39]
	global_load_dword v14, v[14:15], off offset:4
	s_waitcnt vmcnt(0)
	v_cmp_gt_u32_e32 vcc, 64, v14
	s_and_b64 s[34:35], vcc, exec

.LBB1_37:
	s_or_b64 exec, exec, s[8:9]
	s_and_b64 vcc, exec, s[6:7]
	s_cbranch_vccnz .LBB1_41
	s_branch .LBB1_44
.LBB1_39:
	s_endpgm
.LBB1_47:
	s_mul_i32 s2, s33, 0x1388
	s_waitcnt vmcnt(2)
	v_mov_b32_e32 v4, 0
	v_add_u32_e32 v2, s2, v0
	v_mov_b32_e32 v3, v4
	v_or_b32_e32 v33, 0x400, v0
	s_waitcnt vmcnt(1) lgkmcnt(0)
	v_lshl_add_u64 v[6:7], v[2:3], 3, s[38:39]
	v_add_u32_e32 v2, s2, v33
	v_or_b32_e32 v31, 0x800, v0
	v_lshl_add_u64 v[8:9], v[2:3], 3, s[38:39]
	v_add_u32_e32 v2, s2, v31
	v_or_b32_e32 v29, 0xc00, v0
	s_waitcnt vmcnt(0)
	v_lshl_add_u64 v[10:11], v[2:3], 3, s[38:39]
	v_add_u32_e32 v2, s2, v29
	v_lshl_add_u64 v[12:13], v[2:3], 3, s[38:39]
	global_load_dwordx2 v[2:3], v[6:7], off
	global_load_dwordx2 v[24:25], v[8:9], off
	global_load_dwordx2 v[22:23], v[10:11], off
	global_load_dwordx2 v[20:21], v[12:13], off
	s_movk_i32 s0, 0x1388
	v_or_b32_e32 v28, 0x1000, v0
	v_cmp_gt_u32_e32 vcc, s0, v28
	v_mov_b32_e32 v19, 64
	v_mov_b32_e32 v18, 0
	s_and_saveexec_b64 s[0:1], vcc
	s_cbranch_execz .LBB1_49
	v_add_u32_e32 v6, s2, v28
	v_mov_b32_e32 v7, 0
	v_lshl_add_u64 v[6:7], v[6:7], 3, s[38:39]
	global_load_dwordx2 v[18:19], v[6:7], off

.LBB1_94:
	s_and_b64 vcc, exec, s[0:1]
	s_cbranch_vccnz .Lk2_b95
	s_endpgm
.Lk2_b95:
	v_cmp_ne_u32_e64 s[30:31], 0, v2
	s_waitcnt lgkmcnt(0)
	v_add_u32_e32 v35, v27, v27
	s_barrier
	s_and_saveexec_b64 s[0:1], s[30:31]
	ds_write_b64 v35, v[2:3] offset:8224
	s_or_b64 exec, exec, s[0:1]
	v_cndmask_b32_e64 v2, 0, 1, s[30:31]
	v_cmp_eq_u32_e32 vcc, 0, v1
	v_cmp_ne_u32_e64 s[0:1], 0, v2
	s_and_saveexec_b64 s[2:3], vcc
	s_bcnt1_i32_b64 s4, s[0:1]
	v_mov_b32_e32 v2, s4
	ds_write_b32 v30, v2 offset:48224
	s_or_b64 exec, exec, s[2:3]
	v_lshlrev_b64 v[2:3], v1, -1
	v_not_b32_e32 v26, v2
	v_not_b32_e32 v1, v3
	v_and_b32_e32 v3, s0, v26
	v_and_b32_e32 v2, s1, v1
	v_bcnt_u32_b32 v3, v3, 0
	v_bcnt_u32_b32 v36, v2, v3
	v_mov_b32_e32 v2, 0
	s_waitcnt lgkmcnt(0)
	s_barrier
	ds_read_b128 v[14:17], v2 offset:48224
	ds_read_b128 v[10:13], v2 offset:48240
	ds_read_b128 v[6:9], v2 offset:48256
	ds_read_b128 v[2:5], v2 offset:48272
	s_movk_i32 s2, 0x7f
	s_movk_i32 s4, 0xbf
	v_cmp_gt_u32_e64 s[0:1], 64, v0
	s_movk_i32 s6, 0xff
	s_movk_i32 s8, 0x13f
	s_waitcnt lgkmcnt(3)
	v_cndmask_b32_e64 v37, v14, 0, s[0:1]
	v_cmp_lt_u32_e64 s[2:3], s2, v0
	v_cmp_lt_u32_e64 s[4:5], s4, v0
	s_movk_i32 s10, 0x17f
	s_movk_i32 s12, 0x1bf
	v_cndmask_b32_e64 v38, 0, v15, s[2:3]
	v_cndmask_b32_e64 v39, 0, v16, s[4:5]
	v_cmp_lt_u32_e64 s[6:7], s6, v0
	v_cmp_lt_u32_e64 s[8:9], s8, v0
	v_add_u32_e32 v36, v37, v36
	s_movk_i32 s14, 0x1ff
	s_movk_i32 s16, 0x23f
	v_cndmask_b32_e64 v40, 0, v17, s[6:7]
	s_waitcnt lgkmcnt(2)
	v_cndmask_b32_e64 v41, 0, v10, s[8:9]
	v_cmp_lt_u32_e64 s[10:11], s10, v0
	v_cmp_lt_u32_e64 s[12:13], s12, v0
	v_add3_u32 v36, v36, v38, v39
	s_movk_i32 s18, 0x27f
	s_movk_i32 s20, 0x2bf
	v_cndmask_b32_e64 v42, 0, v11, s[10:11]
	v_cndmask_b32_e64 v43, 0, v12, s[12:13]
	v_cmp_lt_u32_e64 s[14:15], s14, v0
	v_cmp_lt_u32_e64 s[16:17], s16, v0
	v_add3_u32 v36, v36, v40, v41
	s_movk_i32 s22, 0x2ff
	s_movk_i32 s24, 0x33f
	v_cndmask_b32_e64 v44, 0, v13, s[14:15]
	s_waitcnt lgkmcnt(1)
	v_cndmask_b32_e64 v45, 0, v6, s[16:17]
	v_cmp_lt_u32_e64 s[18:19], s18, v0
	v_cmp_lt_u32_e64 s[20:21], s20, v0
	v_add3_u32 v36, v36, v42, v43
	s_movk_i32 s26, 0x37f
	v_cndmask_b32_e64 v46, 0, v7, s[18:19]
	v_cndmask_b32_e64 v47, 0, v8, s[20:21]
	v_cmp_lt_u32_e64 s[22:23], s22, v0
	v_cmp_lt_u32_e64 s[24:25], s24, v0
	v_add3_u32 v36, v36, v44, v45
	v_cndmask_b32_e64 v48, 0, v9, s[22:23]
	s_waitcnt lgkmcnt(0)
	v_cndmask_b32_e64 v49, 0, v2, s[24:25]
	v_cmp_lt_u32_e64 s[26:27], s26, v0
	v_cmp_eq_u32_e64 s[28:29], 15, v34
	v_add3_u32 v36, v36, v46, v47
	v_cndmask_b32_e64 v50, 0, v3, s[26:27]
	v_cndmask_b32_e64 v34, 0, v4, s[28:29]
	v_add3_u32 v36, v36, v48, v49
	v_add3_u32 v34, v36, v50, v34
	s_movk_i32 s33, 0x12c
	v_cmp_gt_i32_e64 s[34:35], s33, v34
	s_and_b64 s[34:35], s[30:31], s[34:35]
	s_and_saveexec_b64 s[30:31], s[34:35]
	v_lshlrev_b32_e32 v34, 2, v34
	ds_write_b32 v34, v0 offset:48464
	s_or_b64 exec, exec, s[30:31]
	v_cmp_ne_u32_e64 s[30:31], 0, v24
	s_waitcnt lgkmcnt(0)
	s_barrier
	s_and_saveexec_b64 s[34:35], s[30:31]
	ds_write_b64 v35, v[24:25] offset:16416
	s_or_b64 exec, exec, s[34:35]
	v_cndmask_b32_e64 v24, 0, 1, s[30:31]
	v_cmp_ne_u32_e64 s[34:35], 0, v24
	s_and_saveexec_b64 s[40:41], vcc
	s_bcnt1_i32_b64 s33, s[34:35]
	v_mov_b32_e32 v24, s33
	ds_write_b32 v30, v24 offset:48224
	s_or_b64 exec, exec, s[40:41]
	v_add_u32_e32 v14, v15, v14
	v_add_u32_e32 v14, v14, v16
	v_add_u32_e32 v14, v14, v17
	v_add_u32_e32 v10, v14, v10
	v_add_u32_e32 v10, v10, v11
	v_add_u32_e32 v10, v10, v12
	v_add_u32_e32 v10, v10, v13
	v_add_u32_e32 v6, v10, v6
	v_add_u32_e32 v6, v6, v7
	v_mov_b32_e32 v34, 0
	v_add_u32_e32 v6, v6, v8
	v_add_u32_e32 v6, v6, v9
	s_waitcnt lgkmcnt(0)
	s_barrier
	ds_read_b128 v[14:17], v34 offset:48224
	v_add_u32_e32 v2, v6, v2
	v_and_b32_e32 v25, s34, v26
	v_add_u32_e32 v2, v2, v3
	v_and_b32_e32 v24, s35, v1
	v_bcnt_u32_b32 v25, v25, 0
	v_add_u32_e32 v2, v2, v4
	v_bcnt_u32_b32 v25, v24, v25
	v_add_u32_e32 v24, v2, v5
	ds_read_b128 v[10:13], v34 offset:48240
	ds_read_b128 v[6:9], v34 offset:48256
	ds_read_b128 v[2:5], v34 offset:48272
	s_waitcnt lgkmcnt(3)
	v_cndmask_b32_e64 v34, v14, 0, s[0:1]
	v_cndmask_b32_e64 v36, 0, v15, s[2:3]
	v_cndmask_b32_e64 v37, 0, v16, s[4:5]
	v_add3_u32 v25, v24, v25, v34
	v_cndmask_b32_e64 v38, 0, v17, s[6:7]
	s_waitcnt lgkmcnt(2)
	v_cndmask_b32_e64 v39, 0, v10, s[8:9]
	v_add3_u32 v25, v25, v36, v37
	v_cndmask_b32_e64 v40, 0, v11, s[10:11]
	v_cndmask_b32_e64 v41, 0, v12, s[12:13]
	v_add3_u32 v25, v25, v38, v39
	v_cndmask_b32_e64 v42, 0, v13, s[14:15]
	s_waitcnt lgkmcnt(1)
	v_cndmask_b32_e64 v43, 0, v6, s[16:17]
	v_add3_u32 v25, v25, v40, v41
	v_cndmask_b32_e64 v44, 0, v7, s[18:19]
	v_cndmask_b32_e64 v45, 0, v8, s[20:21]
	v_add3_u32 v25, v25, v42, v43
	v_cndmask_b32_e64 v46, 0, v9, s[22:23]
	s_waitcnt lgkmcnt(0)
	v_cndmask_b32_e64 v47, 0, v2, s[24:25]
	v_add3_u32 v25, v25, v44, v45
	v_cndmask_b32_e64 v48, 0, v3, s[26:27]
	v_cndmask_b32_e64 v49, 0, v4, s[28:29]
	v_add3_u32 v25, v25, v46, v47
	v_add3_u32 v25, v25, v48, v49
	s_movk_i32 s33, 0x12c
	v_cmp_gt_i32_e64 s[34:35], s33, v25
	s_and_b64 s[34:35], s[30:31], s[34:35]
	s_and_saveexec_b64 s[30:31], s[34:35]
	v_lshlrev_b32_e32 v25, 2, v25
	ds_write_b32 v25, v33 offset:48464
	s_or_b64 exec, exec, s[30:31]
	v_cmp_ne_u32_e64 s[30:31], 0, v22
	s_waitcnt lgkmcnt(0)
	s_barrier
	s_and_saveexec_b64 s[34:35], s[30:31]
	ds_write_b64 v35, v[22:23] offset:24608
	s_or_b64 exec, exec, s[34:35]
	v_cndmask_b32_e64 v22, 0, 1, s[30:31]
	v_cmp_ne_u32_e64 s[34:35], 0, v22
	s_and_saveexec_b64 s[40:41], vcc
	s_bcnt1_i32_b64 s33, s[34:35]
	v_mov_b32_e32 v22, s33
	ds_write_b32 v30, v22 offset:48224
	s_or_b64 exec, exec, s[40:41]
	v_add_u32_e32 v14, v14, v24
	v_add_u32_e32 v14, v14, v15
	v_add_u32_e32 v14, v14, v16
	v_add_u32_e32 v14, v14, v17
	v_add_u32_e32 v10, v14, v10
	v_add_u32_e32 v10, v10, v11
	v_add_u32_e32 v10, v10, v12
	v_add_u32_e32 v10, v10, v13
	v_add_u32_e32 v6, v10, v6
	v_add_u32_e32 v6, v6, v7
	v_mov_b32_e32 v25, 0
	v_add_u32_e32 v6, v6, v8
	v_add_u32_e32 v6, v6, v9
	s_waitcnt lgkmcnt(0)
	s_barrier
	ds_read_b128 v[14:17], v25 offset:48224
	v_add_u32_e32 v2, v6, v2
	v_and_b32_e32 v23, s34, v26
	v_add_u32_e32 v2, v2, v3
	v_and_b32_e32 v22, s35, v1
	v_bcnt_u32_b32 v23, v23, 0
	v_add_u32_e32 v2, v2, v4
	v_bcnt_u32_b32 v23, v22, v23
	v_add_u32_e32 v22, v2, v5
	ds_read_b128 v[10:13], v25 offset:48240
	ds_read_b128 v[6:9], v25 offset:48256
	ds_read_b128 v[2:5], v25 offset:48272
	s_waitcnt lgkmcnt(3)
	v_cndmask_b32_e64 v24, v14, 0, s[0:1]
	v_cndmask_b32_e64 v25, 0, v15, s[2:3]
	v_cndmask_b32_e64 v33, 0, v16, s[4:5]
	v_add3_u32 v23, v22, v23, v24
	v_cndmask_b32_e64 v34, 0, v17, s[6:7]
	s_waitcnt lgkmcnt(2)
	v_cndmask_b32_e64 v36, 0, v10, s[8:9]
	v_add3_u32 v23, v23, v25, v33
	v_cndmask_b32_e64 v37, 0, v11, s[10:11]
	v_cndmask_b32_e64 v38, 0, v12, s[12:13]
	v_add3_u32 v23, v23, v34, v36
	v_cndmask_b32_e64 v39, 0, v13, s[14:15]
	s_waitcnt lgkmcnt(1)
	v_cndmask_b32_e64 v40, 0, v6, s[16:17]
	v_add3_u32 v23, v23, v37, v38
	v_cndmask_b32_e64 v41, 0, v7, s[18:19]
	v_cndmask_b32_e64 v42, 0, v8, s[20:21]
	v_add3_u32 v23, v23, v39, v40
	v_cndmask_b32_e64 v43, 0, v9, s[22:23]
	s_waitcnt lgkmcnt(0)
	v_cndmask_b32_e64 v44, 0, v2, s[24:25]
	v_add3_u32 v23, v23, v41, v42
	v_cndmask_b32_e64 v45, 0, v3, s[26:27]
	v_cndmask_b32_e64 v46, 0, v4, s[28:29]
	v_add3_u32 v23, v23, v43, v44
	v_add3_u32 v23, v23, v45, v46
	s_movk_i32 s33, 0x12c
	v_cmp_gt_i32_e64 s[34:35], s33, v23
	s_and_b64 s[34:35], s[30:31], s[34:35]
	s_and_saveexec_b64 s[30:31], s[34:35]
	v_lshlrev_b32_e32 v23, 2, v23
	ds_write_b32 v23, v31 offset:48464
	s_or_b64 exec, exec, s[30:31]
	v_cmp_ne_u32_e64 s[30:31], 0, v20
	s_waitcnt lgkmcnt(0)
	s_barrier
	s_and_saveexec_b64 s[34:35], s[30:31]
	ds_write_b64 v35, v[20:21] offset:32800
	s_or_b64 exec, exec, s[34:35]
	v_cndmask_b32_e64 v20, 0, 1, s[30:31]
	v_cmp_ne_u32_e64 s[34:35], 0, v20
	s_and_saveexec_b64 s[40:41], vcc
	s_bcnt1_i32_b64 s33, s[34:35]
	v_mov_b32_e32 v20, s33
	ds_write_b32 v30, v20 offset:48224
	s_or_b64 exec, exec, s[40:41]
	v_add_u32_e32 v14, v14, v22
	v_add_u32_e32 v14, v14, v15
	v_add_u32_e32 v14, v14, v16
	v_add_u32_e32 v14, v14, v17
	v_add_u32_e32 v10, v14, v10
	v_add_u32_e32 v10, v10, v11
	v_add_u32_e32 v10, v10, v12
	v_add_u32_e32 v10, v10, v13
	v_add_u32_e32 v6, v10, v6
	v_add_u32_e32 v6, v6, v7
	v_mov_b32_e32 v23, 0
	v_add_u32_e32 v6, v6, v8
	v_add_u32_e32 v6, v6, v9
	s_waitcnt lgkmcnt(0)
	s_barrier
	ds_read_b128 v[14:17], v23 offset:48224
	v_add_u32_e32 v2, v6, v2
	v_and_b32_e32 v21, s34, v26
	v_add_u32_e32 v2, v2, v3
	v_and_b32_e32 v20, s35, v1
	v_bcnt_u32_b32 v21, v21, 0
	v_add_u32_e32 v2, v2, v4
	v_bcnt_u32_b32 v21, v20, v21
	v_add_u32_e32 v20, v2, v5
	ds_read_b128 v[10:13], v23 offset:48240
	ds_read_b128 v[6:9], v23 offset:48256
	ds_read_b128 v[2:5], v23 offset:48272
	s_waitcnt lgkmcnt(3)
	v_cndmask_b32_e64 v22, v14, 0, s[0:1]
	v_cndmask_b32_e64 v23, 0, v15, s[2:3]
	v_cndmask_b32_e64 v24, 0, v16, s[4:5]
	v_add3_u32 v21, v20, v21, v22
	v_cndmask_b32_e64 v25, 0, v17, s[6:7]
	s_waitcnt lgkmcnt(2)
	v_cndmask_b32_e64 v31, 0, v10, s[8:9]
	v_add3_u32 v21, v21, v23, v24
	v_cndmask_b32_e64 v33, 0, v11, s[10:11]
	v_cndmask_b32_e64 v34, 0, v12, s[12:13]
	v_add3_u32 v21, v21, v25, v31
	v_cndmask_b32_e64 v36, 0, v13, s[14:15]
	s_waitcnt lgkmcnt(1)
	v_cndmask_b32_e64 v37, 0, v6, s[16:17]
	v_add3_u32 v21, v21, v33, v34
	v_cndmask_b32_e64 v38, 0, v7, s[18:19]
	v_cndmask_b32_e64 v39, 0, v8, s[20:21]
	v_add3_u32 v21, v21, v36, v37
	v_cndmask_b32_e64 v40, 0, v9, s[22:23]
	s_waitcnt lgkmcnt(0)
	v_cndmask_b32_e64 v41, 0, v2, s[24:25]
	v_add3_u32 v21, v21, v38, v39
	v_cndmask_b32_e64 v42, 0, v3, s[26:27]
	v_cndmask_b32_e64 v43, 0, v4, s[28:29]
	v_add3_u32 v21, v21, v40, v41
	v_add3_u32 v21, v21, v42, v43
	s_movk_i32 s33, 0x12c
	v_cmp_gt_i32_e64 s[34:35], s33, v21
	s_and_b64 s[34:35], s[30:31], s[34:35]
	s_and_saveexec_b64 s[30:31], s[34:35]
	v_lshlrev_b32_e32 v21, 2, v21
	ds_write_b32 v21, v29 offset:48464
	s_or_b64 exec, exec, s[30:31]
	v_cmp_ne_u32_e64 s[30:31], 0, v18
	s_waitcnt lgkmcnt(0)
	s_barrier
	s_and_saveexec_b64 s[34:35], s[30:31]
	ds_write_b64 v35, v[18:19] offset:40992
	s_or_b64 exec, exec, s[34:35]
	v_cndmask_b32_e64 v18, 0, 1, s[30:31]
	v_cmp_ne_u32_e64 s[34:35], 0, v18
	s_and_saveexec_b64 s[40:41], vcc
	s_bcnt1_i32_b64 s33, s[34:35]
	v_mov_b32_e32 v18, s33
	ds_write_b32 v30, v18 offset:48224
	s_or_b64 exec, exec, s[40:41]
	v_add_u32_e32 v14, v14, v20
	v_add_u32_e32 v14, v14, v15
	v_add_u32_e32 v14, v14, v16
	v_add_u32_e32 v14, v14, v17
	v_add_u32_e32 v10, v14, v10
	v_add_u32_e32 v10, v10, v11
	v_add_u32_e32 v10, v10, v12
	v_add_u32_e32 v10, v10, v13
	v_add_u32_e32 v6, v10, v6
	v_and_b32_e32 v18, s34, v26
	v_add_u32_e32 v6, v6, v7
	v_and_b32_e32 v1, s35, v1
	v_bcnt_u32_b32 v18, v18, 0
	v_add_u32_e32 v6, v6, v8
	v_bcnt_u32_b32 v1, v1, v18
	v_mov_b32_e32 v18, 0
	v_add_u32_e32 v6, v6, v9
	v_add_u32_e32 v2, v6, v2
	s_waitcnt lgkmcnt(0)
	s_barrier
	ds_read_b128 v[6:9], v18 offset:48224
	v_add_u32_e32 v2, v2, v3
	v_add_u32_e32 v2, v2, v4
	v_add_u32_e32 v17, v2, v5
	ds_read_b128 v[2:5], v18 offset:48240
	ds_read_b128 v[10:13], v18 offset:48256
	ds_read_b96 v[14:16], v18 offset:48272
	s_waitcnt lgkmcnt(3)
	v_cndmask_b32_e64 v6, v6, 0, s[0:1]
	v_cndmask_b32_e64 v7, 0, v7, s[2:3]
	v_cndmask_b32_e64 v8, 0, v8, s[4:5]
	v_add3_u32 v1, v17, v1, v6
	v_cndmask_b32_e64 v9, 0, v9, s[6:7]
	s_waitcnt lgkmcnt(2)
	v_cndmask_b32_e64 v2, 0, v2, s[8:9]
	v_add3_u32 v1, v1, v7, v8
	v_cndmask_b32_e64 v3, 0, v3, s[10:11]
	v_cndmask_b32_e64 v4, 0, v4, s[12:13]
	v_add3_u32 v1, v1, v9, v2
	v_cndmask_b32_e64 v5, 0, v5, s[14:15]
	s_waitcnt lgkmcnt(1)
	v_cndmask_b32_e64 v10, 0, v10, s[16:17]
	v_add3_u32 v1, v1, v3, v4
	v_cndmask_b32_e64 v11, 0, v11, s[18:19]
	v_cndmask_b32_e64 v12, 0, v12, s[20:21]
	v_add3_u32 v1, v1, v5, v10
	v_cndmask_b32_e64 v13, 0, v13, s[22:23]
	s_waitcnt lgkmcnt(0)
	v_cndmask_b32_e64 v14, 0, v14, s[24:25]
	v_add3_u32 v1, v1, v11, v12
	v_cndmask_b32_e64 v15, 0, v15, s[26:27]
	v_cndmask_b32_e64 v16, 0, v16, s[28:29]
	v_add3_u32 v1, v1, v13, v14
	v_add3_u32 v1, v1, v15, v16
	s_movk_i32 s2, 0x12c
	v_cmp_gt_i32_e32 vcc, s2, v1
	s_and_b64 s[4:5], s[30:31], vcc
	s_and_saveexec_b64 s[0:1], s[4:5]
	v_lshlrev_b32_e32 v1, 2, v1
	ds_write_b32 v1, v28 offset:48464
	s_or_b64 exec, exec, s[0:1]
	v_cmp_gt_u32_e32 vcc, s2, v0
	s_waitcnt lgkmcnt(0)
	s_barrier
	s_and_saveexec_b64 s[0:1], vcc
	s_cbranch_execz .LBB1_39
	v_cmp_ge_i32_e32 vcc, v0, v32
	v_mul_u32_u24_e32 v0, 3, v0
	s_and_saveexec_b64 s[0:1], vcc
	s_xor_b64 s[0:1], exec, s[0:1]
	s_cbranch_execz .LBB1_129
	v_lshlrev_b32_e32 v3, 2, v0
	v_mov_b32_e32 v0, -1.0
	v_mov_b32_e32 v2, 0
	v_mov_b32_e32 v1, v0
	global_store_dwordx3 v3, v[0:2], s[38:39]
	s_or_saveexec_b64 s[0:1], s[0:1]
	s_nop 0
	v_mov_b32_e32 v1, 0
	s_xor_b64 exec, exec, s[0:1]
	s_cbranch_execnz .LBB1_130

	.amdhsa_kernel _Z13select_kernelPK15HIP_vector_typeIjLj2EEPKfPf
		.amdhsa_group_segment_fixed_size 49664
		.amdhsa_private_segment_fixed_size 0
		.amdhsa_kernarg_size 24
		.amdhsa_user_sgpr_count 2
		.amdhsa_user_sgpr_dispatch_ptr 0
		.amdhsa_user_sgpr_queue_ptr 0
		.amdhsa_user_sgpr_kernarg_segment_ptr 1
		.amdhsa_user_sgpr_dispatch_id 0
		.amdhsa_user_sgpr_kernarg_preload_length 0
		.amdhsa_user_sgpr_kernarg_preload_offset 0
		.amdhsa_user_sgpr_private_segment_size 0
		.amdhsa_uses_dynamic_stack 0
		.amdhsa_enable_private_segment 0
		.amdhsa_system_sgpr_workgroup_id_x 1
		.amdhsa_system_sgpr_workgroup_id_y 0
		.amdhsa_system_sgpr_workgroup_id_z 0
		.amdhsa_system_sgpr_workgroup_info 0
		.amdhsa_system_vgpr_workitem_id 0
		.amdhsa_next_free_vgpr 58
		.amdhsa_next_free_sgpr 52
		.amdhsa_accum_offset 60
		.amdhsa_reserve_vcc 1
		.amdhsa_float_round_mode_32 0
		.amdhsa_float_round_mode_16_64 0
		.amdhsa_float_denorm_mode_32 3
		.amdhsa_float_denorm_mode_16_64 3
		.amdhsa_dx10_clamp 1
		.amdhsa_ieee_mode 1
		.amdhsa_fp16_overflow 0
		.amdhsa_tg_split 0
		.amdhsa_exception_fp_ieee_invalid_op 0
		.amdhsa_exception_fp_denorm_src 0
		.amdhsa_exception_fp_ieee_div_zero 0
		.amdhsa_exception_fp_ieee_overflow 0
		.amdhsa_exception_fp_ieee_underflow 0
		.amdhsa_exception_fp_ieee_inexact 0
		.amdhsa_exception_int_div_zero 0
	.end_amdhsa_kernel

amdhsa.kernels:
  - .agpr_count:     0
    .args:
      - .actual_access:  read_only
        .address_space:  global
        .offset:         0
        .size:           8
        .value_kind:     global_buffer
      - .actual_access:  write_only
        .address_space:  global
        .offset:         8
        .size:           8
        .value_kind:     global_buffer
      - .actual_access:  read_only
        .address_space:  global
        .offset:         16
        .size:           8
        .value_kind:     global_buffer
      - .actual_access:  read_only
        .address_space:  global
        .offset:         24
        .size:           8
        .value_kind:     global_buffer
    .group_segment_fixed_size: 0
    .kernarg_segment_align: 8
    .kernarg_segment_size: 32
    .language:       OpenCL C
    .language_version:
      - 2
      - 0
    .max_flat_workgroup_size: 640
    .name:           _Z12score_kernelPKfP15HIP_vector_typeIjLj2EES0_S0_
    .private_segment_fixed_size: 0
    .sgpr_count:     62
    .sgpr_spill_count: 0
    .symbol:         _Z12score_kernelPKfP15HIP_vector_typeIjLj2EES0_S0_.kd
    .uniform_work_group_size: 1
    .uses_dynamic_stack: false
    .vgpr_count:     100
    .vgpr_spill_count: 0
    .wavefront_size: 64
  - .agpr_count:     0
    .args:
      - .actual_access:  read_only
        .address_space:  global
        .offset:         0
        .size:           8
        .value_kind:     global_buffer
      - .actual_access:  read_only
        .address_space:  global
        .offset:         8
        .size:           8
        .value_kind:     global_buffer
      - .actual_access:  write_only
        .address_space:  global
        .offset:         16
        .size:           8
        .value_kind:     global_buffer
    .group_segment_fixed_size: 49664
    .kernarg_segment_align: 8
    .kernarg_segment_size: 24
    .language:       OpenCL C
    .language_version:
      - 2
      - 0
    .max_flat_workgroup_size: 1024
    .name:           _Z13select_kernelPK15HIP_vector_typeIjLj2EEPKfPf
    .private_segment_fixed_size: 0
    .sgpr_count:     58
    .sgpr_spill_count: 0
    .symbol:         _Z13select_kernelPK15HIP_vector_typeIjLj2EEPKfPf.kd
    .uniform_work_group_size: 1
    .uses_dynamic_stack: false
    .vgpr_count:     58
    .vgpr_spill_count: 0
    .wavefront_size: 64
